# speedup vs baseline: 1.0096x; 1.0066x over previous
.LBB0_2:
	s_add_i32 s12, s4, 0xffffb000
	s_and_b32 s12, s12, 0x1e000
	s_lshl_b32 s12, s12, 4
	s_waitcnt lgkmcnt(0)
	s_barrier
	v_lshl_add_u64 v[166:167], v[130:131], 0, s[12:13]
	global_load_dwordx4 v[134:137], v[166:167], off
	global_load_dwordx4 v[138:141], v[166:167], off offset:1024
	global_load_dwordx4 v[142:145], v[166:167], off offset:2048
	global_load_dwordx4 v[146:149], v[166:167], off offset:3072
	ds_read_b128 v[150:153], v132
	ds_read_b128 v[154:157], v132 offset:2048
	ds_read_b128 v[158:161], v132 offset:4096
	ds_read_b128 v[162:165], v132 offset:6144
	s_setprio 2
	s_waitcnt vmcnt(19) lgkmcnt(3)
	v_mfma_f32_16x16x32_f16 v[50:53], v[54:57], v[150:153], v[50:53]
	s_waitcnt vmcnt(18)
	v_mfma_f32_16x16x32_f16 v[70:73], v[58:61], v[150:153], v[70:73]
	s_waitcnt vmcnt(17)
	v_mfma_f32_16x16x32_f16 v[74:77], v[62:65], v[150:153], v[74:77]
	s_waitcnt vmcnt(16)
	v_mfma_f32_16x16x32_f16 v[78:81], v[66:69], v[150:153], v[78:81]
	s_waitcnt lgkmcnt(2)
	v_mfma_f32_16x16x32_f16 v[82:85], v[54:57], v[154:157], v[82:85]
	v_mfma_f32_16x16x32_f16 v[86:89], v[58:61], v[154:157], v[86:89]
	v_mfma_f32_16x16x32_f16 v[90:93], v[62:65], v[154:157], v[90:93]
	v_mfma_f32_16x16x32_f16 v[94:97], v[66:69], v[154:157], v[94:97]
	s_waitcnt lgkmcnt(1)
	v_mfma_f32_16x16x32_f16 v[98:101], v[54:57], v[158:161], v[98:101]
	v_mfma_f32_16x16x32_f16 v[102:105], v[58:61], v[158:161], v[102:105]
	v_mfma_f32_16x16x32_f16 v[106:109], v[62:65], v[158:161], v[106:109]
	v_mfma_f32_16x16x32_f16 v[110:113], v[66:69], v[158:161], v[110:113]
	s_waitcnt lgkmcnt(0)
	v_mfma_f32_16x16x32_f16 v[54:57], v[54:57], v[162:165], v[114:117]
	v_mfma_f32_16x16x32_f16 v[58:61], v[58:61], v[162:165], v[118:121]
	v_mfma_f32_16x16x32_f16 v[62:65], v[62:65], v[162:165], v[122:125]
	v_mfma_f32_16x16x32_f16 v[66:69], v[66:69], v[162:165], v[126:129]
	s_setprio 1
	s_nop 1
	v_add_co_u32_e32 v126, vcc, s3, v166
	s_nop 1
	v_addc_co_u32_e32 v127, vcc, 0, v167, vcc
	global_load_dwordx4 v[114:117], v[126:127], off
	global_load_dwordx4 v[118:121], v[126:127], off offset:1024
	global_load_dwordx4 v[122:125], v[126:127], off offset:2048
	s_nop 0
	global_load_dwordx4 v[126:129], v[126:127], off offset:3072
	ds_read_b128 v[150:153], v132 offset:1024
	ds_read_b128 v[154:157], v132 offset:3072
	ds_read_b128 v[158:161], v132 offset:5120
	ds_read_b128 v[162:165], v132 offset:7168
	s_setprio 2
	s_waitcnt vmcnt(19) lgkmcnt(3)
	v_mfma_f32_16x16x32_f16 v[50:53], v[34:37], v[150:153], v[50:53]
	s_waitcnt vmcnt(18)
	v_mfma_f32_16x16x32_f16 v[70:73], v[38:41], v[150:153], v[70:73]
	s_waitcnt vmcnt(17)
	v_mfma_f32_16x16x32_f16 v[74:77], v[42:45], v[150:153], v[74:77]
	s_waitcnt vmcnt(16)
	v_mfma_f32_16x16x32_f16 v[78:81], v[46:49], v[150:153], v[78:81]
	s_waitcnt lgkmcnt(2)
	v_mfma_f32_16x16x32_f16 v[82:85], v[34:37], v[154:157], v[82:85]
	v_mfma_f32_16x16x32_f16 v[86:89], v[38:41], v[154:157], v[86:89]
	v_mfma_f32_16x16x32_f16 v[90:93], v[42:45], v[154:157], v[90:93]
	v_mfma_f32_16x16x32_f16 v[94:97], v[46:49], v[154:157], v[94:97]
	s_waitcnt lgkmcnt(1)
	v_mfma_f32_16x16x32_f16 v[98:101], v[34:37], v[158:161], v[98:101]
	v_mfma_f32_16x16x32_f16 v[102:105], v[38:41], v[158:161], v[102:105]
	v_mfma_f32_16x16x32_f16 v[106:109], v[42:45], v[158:161], v[106:109]
	v_mfma_f32_16x16x32_f16 v[110:113], v[46:49], v[158:161], v[110:113]
	s_waitcnt lgkmcnt(0)
	v_mfma_f32_16x16x32_f16 v[34:37], v[34:37], v[162:165], v[54:57]
	v_mfma_f32_16x16x32_f16 v[38:41], v[38:41], v[162:165], v[58:61]
	v_mfma_f32_16x16x32_f16 v[42:45], v[42:45], v[162:165], v[62:65]
	v_mfma_f32_16x16x32_f16 v[46:49], v[46:49], v[162:165], v[66:69]
	s_setprio 1
	s_add_i32 s12, s4, 0xffffc000
	s_and_b32 s12, s12, 0x1f000
	s_lshl_b32 s12, s12, 4
	s_waitcnt lgkmcnt(0)
	s_barrier
	v_lshl_add_u64 v[166:167], v[130:131], 0, s[12:13]
	global_load_dwordx4 v[54:57], v[166:167], off
	global_load_dwordx4 v[58:61], v[166:167], off offset:1024
	global_load_dwordx4 v[62:65], v[166:167], off offset:2048
	global_load_dwordx4 v[66:69], v[166:167], off offset:3072
	ds_read_b128 v[150:153], v132 offset:8192
	ds_read_b128 v[154:157], v132 offset:10240
	ds_read_b128 v[158:161], v132 offset:12288
	ds_read_b128 v[162:165], v132 offset:14336
	s_setprio 2
	s_waitcnt vmcnt(16) lgkmcnt(3)
	v_mfma_f32_16x16x32_f16 v[50:53], v[30:33], v[150:153], v[50:53]
	v_mfma_f32_16x16x32_f16 v[70:73], v[18:21], v[150:153], v[70:73]
	v_mfma_f32_16x16x32_f16 v[74:77], v[22:25], v[150:153], v[74:77]
	v_mfma_f32_16x16x32_f16 v[78:81], v[26:29], v[150:153], v[78:81]
	s_waitcnt lgkmcnt(2)
	v_mfma_f32_16x16x32_f16 v[82:85], v[30:33], v[154:157], v[82:85]
	v_mfma_f32_16x16x32_f16 v[86:89], v[18:21], v[154:157], v[86:89]
	v_mfma_f32_16x16x32_f16 v[90:93], v[22:25], v[154:157], v[90:93]
	v_mfma_f32_16x16x32_f16 v[94:97], v[26:29], v[154:157], v[94:97]
	s_waitcnt lgkmcnt(1)
	v_mfma_f32_16x16x32_f16 v[98:101], v[30:33], v[158:161], v[98:101]
	v_mfma_f32_16x16x32_f16 v[102:105], v[18:21], v[158:161], v[102:105]
	v_mfma_f32_16x16x32_f16 v[106:109], v[22:25], v[158:161], v[106:109]
	v_mfma_f32_16x16x32_f16 v[110:113], v[26:29], v[158:161], v[110:113]
	s_waitcnt lgkmcnt(0)
	v_mfma_f32_16x16x32_f16 v[30:33], v[30:33], v[162:165], v[34:37]
	v_mfma_f32_16x16x32_f16 v[18:21], v[18:21], v[162:165], v[38:41]
	v_mfma_f32_16x16x32_f16 v[22:25], v[22:25], v[162:165], v[42:45]
	v_mfma_f32_16x16x32_f16 v[26:29], v[26:29], v[162:165], v[46:49]
	s_setprio 1
	s_nop 1
	v_add_co_u32_e32 v46, vcc, s3, v166
	s_nop 1
	v_addc_co_u32_e32 v47, vcc, 0, v167, vcc
	global_load_dwordx4 v[34:37], v[46:47], off
	global_load_dwordx4 v[38:41], v[46:47], off offset:1024
	global_load_dwordx4 v[42:45], v[46:47], off offset:2048
	s_nop 0
	global_load_dwordx4 v[46:49], v[46:47], off offset:3072
	ds_read_b128 v[150:153], v132 offset:9216
	ds_read_b128 v[154:157], v132 offset:11264
	ds_read_b128 v[158:161], v132 offset:13312
	ds_read_b128 v[162:165], v132 offset:15360
	s_setprio 2
	s_waitcnt vmcnt(19) lgkmcnt(3)
	v_mfma_f32_16x16x32_f16 v[50:53], v[2:5], v[150:153], v[50:53]
	s_waitcnt vmcnt(18)
	v_mfma_f32_16x16x32_f16 v[70:73], v[6:9], v[150:153], v[70:73]
	s_waitcnt vmcnt(17)
	v_mfma_f32_16x16x32_f16 v[74:77], v[10:13], v[150:153], v[74:77]
	s_waitcnt vmcnt(16)
	v_mfma_f32_16x16x32_f16 v[78:81], v[14:17], v[150:153], v[78:81]
	s_waitcnt lgkmcnt(2)
	v_mfma_f32_16x16x32_f16 v[82:85], v[2:5], v[154:157], v[82:85]
	v_mfma_f32_16x16x32_f16 v[86:89], v[6:9], v[154:157], v[86:89]
	v_mfma_f32_16x16x32_f16 v[90:93], v[10:13], v[154:157], v[90:93]
	v_mfma_f32_16x16x32_f16 v[94:97], v[14:17], v[154:157], v[94:97]
	s_waitcnt lgkmcnt(1)
	v_mfma_f32_16x16x32_f16 v[98:101], v[2:5], v[158:161], v[98:101]
	v_mfma_f32_16x16x32_f16 v[102:105], v[6:9], v[158:161], v[102:105]
	v_mfma_f32_16x16x32_f16 v[106:109], v[10:13], v[158:161], v[106:109]
	v_mfma_f32_16x16x32_f16 v[110:113], v[14:17], v[158:161], v[110:113]
	s_waitcnt lgkmcnt(0)
	v_mfma_f32_16x16x32_f16 v[2:5], v[2:5], v[162:165], v[30:33]
	v_mfma_f32_16x16x32_f16 v[6:9], v[6:9], v[162:165], v[18:21]
	v_mfma_f32_16x16x32_f16 v[10:13], v[10:13], v[162:165], v[22:25]
	v_mfma_f32_16x16x32_f16 v[14:17], v[14:17], v[162:165], v[26:29]
	s_setprio 1
	s_add_i32 s12, s4, 0xffffd000
	s_and_b32 s12, s12, 0x1e000
	s_lshl_b32 s12, s12, 4
	s_waitcnt lgkmcnt(0)
	s_barrier
	v_lshl_add_u64 v[166:167], v[130:131], 0, s[12:13]
	global_load_dwordx4 v[18:21], v[166:167], off
	global_load_dwordx4 v[22:25], v[166:167], off offset:1024
	global_load_dwordx4 v[26:29], v[166:167], off offset:2048
	global_load_dwordx4 v[30:33], v[166:167], off offset:3072
	ds_read_b128 v[150:153], v132
	ds_read_b128 v[154:157], v132 offset:2048
	ds_read_b128 v[158:161], v132 offset:4096
	ds_read_b128 v[162:165], v132 offset:6144
	s_setprio 2
	s_waitcnt vmcnt(19) lgkmcnt(3)
	v_mfma_f32_16x16x32_f16 v[50:53], v[134:137], v[150:153], v[50:53]
	s_waitcnt vmcnt(18)
	v_mfma_f32_16x16x32_f16 v[70:73], v[138:141], v[150:153], v[70:73]
	s_waitcnt vmcnt(17)
	v_mfma_f32_16x16x32_f16 v[74:77], v[142:145], v[150:153], v[74:77]
	s_waitcnt vmcnt(16)
	v_mfma_f32_16x16x32_f16 v[78:81], v[146:149], v[150:153], v[78:81]
	s_waitcnt lgkmcnt(2)
	v_mfma_f32_16x16x32_f16 v[82:85], v[134:137], v[154:157], v[82:85]
	v_mfma_f32_16x16x32_f16 v[86:89], v[138:141], v[154:157], v[86:89]
	v_mfma_f32_16x16x32_f16 v[90:93], v[142:145], v[154:157], v[90:93]
	v_mfma_f32_16x16x32_f16 v[94:97], v[146:149], v[154:157], v[94:97]
	s_waitcnt lgkmcnt(1)
	v_mfma_f32_16x16x32_f16 v[98:101], v[134:137], v[158:161], v[98:101]
	v_mfma_f32_16x16x32_f16 v[102:105], v[138:141], v[158:161], v[102:105]
	v_mfma_f32_16x16x32_f16 v[106:109], v[142:145], v[158:161], v[106:109]
	v_mfma_f32_16x16x32_f16 v[110:113], v[146:149], v[158:161], v[110:113]
	s_waitcnt lgkmcnt(0)
	v_mfma_f32_16x16x32_f16 v[2:5], v[134:137], v[162:165], v[2:5]
	v_mfma_f32_16x16x32_f16 v[6:9], v[138:141], v[162:165], v[6:9]
	v_mfma_f32_16x16x32_f16 v[10:13], v[142:145], v[162:165], v[10:13]
	v_mfma_f32_16x16x32_f16 v[14:17], v[146:149], v[162:165], v[14:17]
	s_setprio 1
	v_add_co_u32_e32 v146, vcc, s3, v166
	s_nop 1
	v_addc_co_u32_e32 v147, vcc, 0, v167, vcc
	global_load_dwordx4 v[134:137], v[146:147], off
	global_load_dwordx4 v[138:141], v[146:147], off offset:1024
	global_load_dwordx4 v[142:145], v[146:147], off offset:2048
	s_nop 0
	global_load_dwordx4 v[146:149], v[146:147], off offset:3072
	ds_read_b128 v[150:153], v132 offset:1024
	ds_read_b128 v[154:157], v132 offset:3072
	ds_read_b128 v[158:161], v132 offset:5120
	ds_read_b128 v[162:165], v132 offset:7168
	s_setprio 2
	s_waitcnt vmcnt(19) lgkmcnt(3)
	v_mfma_f32_16x16x32_f16 v[50:53], v[114:117], v[150:153], v[50:53]
	s_waitcnt vmcnt(18)
	v_mfma_f32_16x16x32_f16 v[70:73], v[118:121], v[150:153], v[70:73]
	s_waitcnt vmcnt(17)
	v_mfma_f32_16x16x32_f16 v[74:77], v[122:125], v[150:153], v[74:77]
	s_waitcnt vmcnt(16)
	v_mfma_f32_16x16x32_f16 v[78:81], v[126:129], v[150:153], v[78:81]
	s_waitcnt lgkmcnt(2)
	v_mfma_f32_16x16x32_f16 v[82:85], v[114:117], v[154:157], v[82:85]
	v_mfma_f32_16x16x32_f16 v[86:89], v[118:121], v[154:157], v[86:89]
	v_mfma_f32_16x16x32_f16 v[90:93], v[122:125], v[154:157], v[90:93]
	v_mfma_f32_16x16x32_f16 v[94:97], v[126:129], v[154:157], v[94:97]
	s_waitcnt lgkmcnt(1)
	v_mfma_f32_16x16x32_f16 v[98:101], v[114:117], v[158:161], v[98:101]
	v_mfma_f32_16x16x32_f16 v[102:105], v[118:121], v[158:161], v[102:105]
	v_mfma_f32_16x16x32_f16 v[106:109], v[122:125], v[158:161], v[106:109]
	v_mfma_f32_16x16x32_f16 v[110:113], v[126:129], v[158:161], v[110:113]
	s_waitcnt lgkmcnt(0)
	v_mfma_f32_16x16x32_f16 v[2:5], v[114:117], v[162:165], v[2:5]
	v_mfma_f32_16x16x32_f16 v[6:9], v[118:121], v[162:165], v[6:9]
	v_mfma_f32_16x16x32_f16 v[10:13], v[122:125], v[162:165], v[10:13]
	v_mfma_f32_16x16x32_f16 v[14:17], v[126:129], v[162:165], v[14:17]
	s_setprio 1
	s_add_i32 s12, s4, 0xffffe000
	s_and_b32 s12, s12, 0x1f000
	s_lshl_b32 s12, s12, 4
	s_waitcnt lgkmcnt(0)
	s_barrier
	v_lshl_add_u64 v[166:167], v[130:131], 0, s[12:13]
	global_load_dwordx4 v[114:117], v[166:167], off
	global_load_dwordx4 v[118:121], v[166:167], off offset:1024
	global_load_dwordx4 v[122:125], v[166:167], off offset:2048
	global_load_dwordx4 v[126:129], v[166:167], off offset:3072
	ds_read_b128 v[150:153], v132 offset:8192
	ds_read_b128 v[154:157], v132 offset:10240
	ds_read_b128 v[158:161], v132 offset:12288
	ds_read_b128 v[162:165], v132 offset:14336
	s_setprio 2
	s_waitcnt vmcnt(19) lgkmcnt(3)
	v_mfma_f32_16x16x32_f16 v[50:53], v[54:57], v[150:153], v[50:53]
	s_waitcnt vmcnt(18)
	v_mfma_f32_16x16x32_f16 v[70:73], v[58:61], v[150:153], v[70:73]
	s_waitcnt vmcnt(17)
	v_mfma_f32_16x16x32_f16 v[74:77], v[62:65], v[150:153], v[74:77]
	s_waitcnt vmcnt(16)
	v_mfma_f32_16x16x32_f16 v[78:81], v[66:69], v[150:153], v[78:81]
	s_waitcnt lgkmcnt(2)
	v_mfma_f32_16x16x32_f16 v[82:85], v[54:57], v[154:157], v[82:85]
	v_mfma_f32_16x16x32_f16 v[86:89], v[58:61], v[154:157], v[86:89]
	v_mfma_f32_16x16x32_f16 v[90:93], v[62:65], v[154:157], v[90:93]
	v_mfma_f32_16x16x32_f16 v[94:97], v[66:69], v[154:157], v[94:97]
	s_waitcnt lgkmcnt(1)
	v_mfma_f32_16x16x32_f16 v[98:101], v[54:57], v[158:161], v[98:101]
	v_mfma_f32_16x16x32_f16 v[102:105], v[58:61], v[158:161], v[102:105]
	v_mfma_f32_16x16x32_f16 v[106:109], v[62:65], v[158:161], v[106:109]
	v_mfma_f32_16x16x32_f16 v[110:113], v[66:69], v[158:161], v[110:113]
	s_waitcnt lgkmcnt(0)
	v_mfma_f32_16x16x32_f16 v[2:5], v[54:57], v[162:165], v[2:5]
	v_mfma_f32_16x16x32_f16 v[6:9], v[58:61], v[162:165], v[6:9]
	v_mfma_f32_16x16x32_f16 v[10:13], v[62:65], v[162:165], v[10:13]
	v_mfma_f32_16x16x32_f16 v[14:17], v[66:69], v[162:165], v[14:17]
	s_setprio 1
	v_add_co_u32_e32 v54, vcc, s3, v166
	s_nop 1
	v_addc_co_u32_e32 v55, vcc, 0, v167, vcc
	global_load_dwordx4 v[150:153], v[54:55], off
	global_load_dwordx4 v[154:157], v[54:55], off offset:1024
	global_load_dwordx4 v[158:161], v[54:55], off offset:2048
	global_load_dwordx4 v[162:165], v[54:55], off offset:3072
	ds_read_b128 v[54:57], v132 offset:9216
	ds_read_b128 v[58:61], v132 offset:11264
	ds_read_b128 v[62:65], v132 offset:13312
	ds_read_b128 v[66:69], v132 offset:15360
	s_setprio 2
	s_waitcnt vmcnt(19) lgkmcnt(3)
	v_mfma_f32_16x16x32_f16 v[50:53], v[34:37], v[54:57], v[50:53]
	s_waitcnt vmcnt(18)
	v_mfma_f32_16x16x32_f16 v[70:73], v[38:41], v[54:57], v[70:73]
	s_waitcnt vmcnt(17)
	v_mfma_f32_16x16x32_f16 v[74:77], v[42:45], v[54:57], v[74:77]
	s_waitcnt vmcnt(16)
	v_mfma_f32_16x16x32_f16 v[78:81], v[46:49], v[54:57], v[78:81]
	s_waitcnt lgkmcnt(2)
	v_mfma_f32_16x16x32_f16 v[82:85], v[34:37], v[58:61], v[82:85]
	v_mfma_f32_16x16x32_f16 v[86:89], v[38:41], v[58:61], v[86:89]
	v_mfma_f32_16x16x32_f16 v[90:93], v[42:45], v[58:61], v[90:93]
	v_mfma_f32_16x16x32_f16 v[94:97], v[46:49], v[58:61], v[94:97]
	s_waitcnt lgkmcnt(1)
	v_mfma_f32_16x16x32_f16 v[98:101], v[34:37], v[62:65], v[98:101]
	v_mfma_f32_16x16x32_f16 v[102:105], v[38:41], v[62:65], v[102:105]
	v_mfma_f32_16x16x32_f16 v[106:109], v[42:45], v[62:65], v[106:109]
	v_mfma_f32_16x16x32_f16 v[110:113], v[46:49], v[62:65], v[110:113]
	s_waitcnt lgkmcnt(0)
	v_mfma_f32_16x16x32_f16 v[2:5], v[34:37], v[66:69], v[2:5]
	v_mfma_f32_16x16x32_f16 v[6:9], v[38:41], v[66:69], v[6:9]
	v_mfma_f32_16x16x32_f16 v[10:13], v[42:45], v[66:69], v[10:13]
	v_mfma_f32_16x16x32_f16 v[14:17], v[46:49], v[66:69], v[14:17]
	s_setprio 1
	s_add_i32 s12, s4, 0xfffff000
	s_and_b32 s12, s12, 0x1e000
	s_lshl_b32 s12, s12, 4
	s_waitcnt lgkmcnt(0)
	s_barrier
	v_lshl_add_u64 v[166:167], v[130:131], 0, s[12:13]
	global_load_dwordx4 v[54:57], v[166:167], off
	global_load_dwordx4 v[58:61], v[166:167], off offset:1024
	global_load_dwordx4 v[62:65], v[166:167], off offset:2048
	global_load_dwordx4 v[66:69], v[166:167], off offset:3072
	ds_read_b128 v[34:37], v132
	ds_read_b128 v[38:41], v132 offset:2048
	ds_read_b128 v[42:45], v132 offset:4096
	ds_read_b128 v[46:49], v132 offset:6144
	s_setprio 2
	s_waitcnt vmcnt(19) lgkmcnt(3)
	v_mfma_f32_16x16x32_f16 v[50:53], v[18:21], v[34:37], v[50:53]
	s_waitcnt vmcnt(18)
	v_mfma_f32_16x16x32_f16 v[70:73], v[22:25], v[34:37], v[70:73]
	s_waitcnt vmcnt(17)
	v_mfma_f32_16x16x32_f16 v[74:77], v[26:29], v[34:37], v[74:77]
	s_waitcnt vmcnt(16)
	v_mfma_f32_16x16x32_f16 v[78:81], v[30:33], v[34:37], v[78:81]
	s_waitcnt lgkmcnt(2)
	v_mfma_f32_16x16x32_f16 v[82:85], v[18:21], v[38:41], v[82:85]
	v_mfma_f32_16x16x32_f16 v[86:89], v[22:25], v[38:41], v[86:89]
	v_mfma_f32_16x16x32_f16 v[90:93], v[26:29], v[38:41], v[90:93]
	v_mfma_f32_16x16x32_f16 v[94:97], v[30:33], v[38:41], v[94:97]
	s_waitcnt lgkmcnt(1)
	v_mfma_f32_16x16x32_f16 v[98:101], v[18:21], v[42:45], v[98:101]
	v_mfma_f32_16x16x32_f16 v[102:105], v[22:25], v[42:45], v[102:105]
	v_mfma_f32_16x16x32_f16 v[106:109], v[26:29], v[42:45], v[106:109]
	v_mfma_f32_16x16x32_f16 v[110:113], v[30:33], v[42:45], v[110:113]
	s_waitcnt lgkmcnt(0)
	v_mfma_f32_16x16x32_f16 v[2:5], v[18:21], v[46:49], v[2:5]
	v_mfma_f32_16x16x32_f16 v[6:9], v[22:25], v[46:49], v[6:9]
	v_mfma_f32_16x16x32_f16 v[10:13], v[26:29], v[46:49], v[10:13]
	v_mfma_f32_16x16x32_f16 v[14:17], v[30:33], v[46:49], v[14:17]
	s_setprio 1
	v_add_co_u32_e32 v18, vcc, s3, v166
	s_nop 1
	v_addc_co_u32_e32 v19, vcc, 0, v167, vcc
	global_load_dwordx4 v[34:37], v[18:19], off
	global_load_dwordx4 v[38:41], v[18:19], off offset:1024
	global_load_dwordx4 v[42:45], v[18:19], off offset:2048
	global_load_dwordx4 v[46:49], v[18:19], off offset:3072
	ds_read_b128 v[18:21], v132 offset:1024
	ds_read_b128 v[22:25], v132 offset:3072
	ds_read_b128 v[26:29], v132 offset:5120
	ds_read_b128 v[30:33], v132 offset:7168
	s_setprio 2
	s_waitcnt vmcnt(19) lgkmcnt(3)
	v_mfma_f32_16x16x32_f16 v[50:53], v[134:137], v[18:21], v[50:53]
	s_waitcnt vmcnt(18)
	v_mfma_f32_16x16x32_f16 v[70:73], v[138:141], v[18:21], v[70:73]
	s_waitcnt vmcnt(17)
	v_mfma_f32_16x16x32_f16 v[74:77], v[142:145], v[18:21], v[74:77]
	s_waitcnt vmcnt(16)
	v_mfma_f32_16x16x32_f16 v[78:81], v[146:149], v[18:21], v[78:81]
	s_waitcnt lgkmcnt(2)
	v_mfma_f32_16x16x32_f16 v[82:85], v[134:137], v[22:25], v[82:85]
	v_mfma_f32_16x16x32_f16 v[86:89], v[138:141], v[22:25], v[86:89]
	v_mfma_f32_16x16x32_f16 v[90:93], v[142:145], v[22:25], v[90:93]
	v_mfma_f32_16x16x32_f16 v[94:97], v[146:149], v[22:25], v[94:97]
	s_waitcnt lgkmcnt(1)
	v_mfma_f32_16x16x32_f16 v[98:101], v[134:137], v[26:29], v[98:101]
	v_mfma_f32_16x16x32_f16 v[102:105], v[138:141], v[26:29], v[102:105]
	v_mfma_f32_16x16x32_f16 v[106:109], v[142:145], v[26:29], v[106:109]
	v_mfma_f32_16x16x32_f16 v[110:113], v[146:149], v[26:29], v[110:113]
	s_waitcnt lgkmcnt(0)
	v_mfma_f32_16x16x32_f16 v[2:5], v[134:137], v[30:33], v[2:5]
	v_mfma_f32_16x16x32_f16 v[6:9], v[138:141], v[30:33], v[6:9]
	v_mfma_f32_16x16x32_f16 v[10:13], v[142:145], v[30:33], v[10:13]
	v_mfma_f32_16x16x32_f16 v[14:17], v[146:149], v[30:33], v[14:17]
	s_setprio 1
	s_and_b32 s12, s4, 0x1f000
	s_lshl_b32 s12, s12, 4
	s_waitcnt lgkmcnt(0)
	s_barrier
	v_lshl_add_u64 v[166:167], v[130:131], 0, s[12:13]
	global_load_dwordx4 v[30:33], v[166:167], off
	global_load_dwordx4 v[18:21], v[166:167], off offset:1024
	global_load_dwordx4 v[22:25], v[166:167], off offset:2048
	global_load_dwordx4 v[26:29], v[166:167], off offset:3072
	ds_read_b128 v[134:137], v132 offset:8192
	ds_read_b128 v[138:141], v132 offset:10240
	ds_read_b128 v[142:145], v132 offset:12288
	ds_read_b128 v[146:149], v132 offset:14336
	s_setprio 2
	s_waitcnt vmcnt(19) lgkmcnt(3)
	v_mfma_f32_16x16x32_f16 v[50:53], v[114:117], v[134:137], v[50:53]
	s_waitcnt vmcnt(18)
	v_mfma_f32_16x16x32_f16 v[70:73], v[118:121], v[134:137], v[70:73]
	s_waitcnt vmcnt(17)
	v_mfma_f32_16x16x32_f16 v[74:77], v[122:125], v[134:137], v[74:77]
	s_waitcnt vmcnt(16)
	v_mfma_f32_16x16x32_f16 v[78:81], v[126:129], v[134:137], v[78:81]
	s_waitcnt lgkmcnt(2)
	v_mfma_f32_16x16x32_f16 v[82:85], v[114:117], v[138:141], v[82:85]
	v_mfma_f32_16x16x32_f16 v[86:89], v[118:121], v[138:141], v[86:89]
	v_mfma_f32_16x16x32_f16 v[90:93], v[122:125], v[138:141], v[90:93]
	v_mfma_f32_16x16x32_f16 v[94:97], v[126:129], v[138:141], v[94:97]
	s_waitcnt lgkmcnt(1)
	v_mfma_f32_16x16x32_f16 v[98:101], v[114:117], v[142:145], v[98:101]
	v_mfma_f32_16x16x32_f16 v[102:105], v[118:121], v[142:145], v[102:105]
	v_mfma_f32_16x16x32_f16 v[106:109], v[122:125], v[142:145], v[106:109]
	v_mfma_f32_16x16x32_f16 v[110:113], v[126:129], v[142:145], v[110:113]
	s_waitcnt lgkmcnt(0)
	v_mfma_f32_16x16x32_f16 v[114:117], v[114:117], v[146:149], v[2:5]
	v_mfma_f32_16x16x32_f16 v[118:121], v[118:121], v[146:149], v[6:9]
	v_mfma_f32_16x16x32_f16 v[122:125], v[122:125], v[146:149], v[10:13]
	v_mfma_f32_16x16x32_f16 v[126:129], v[126:129], v[146:149], v[14:17]
	s_setprio 1
	s_nop 1
	v_add_co_u32_e32 v14, vcc, s3, v166
	s_nop 1
	v_addc_co_u32_e32 v15, vcc, 0, v167, vcc
	global_load_dwordx4 v[2:5], v[14:15], off
	global_load_dwordx4 v[6:9], v[14:15], off offset:1024
	global_load_dwordx4 v[10:13], v[14:15], off offset:2048
	s_nop 0
	global_load_dwordx4 v[14:17], v[14:15], off offset:3072
	ds_read_b128 v[134:137], v132 offset:9216
	ds_read_b128 v[138:141], v132 offset:11264
	ds_read_b128 v[142:145], v132 offset:13312
	ds_read_b128 v[146:149], v132 offset:15360
	s_setprio 2
	s_waitcnt vmcnt(19) lgkmcnt(3)
	v_mfma_f32_16x16x32_f16 v[50:53], v[150:153], v[134:137], v[50:53]
	s_waitcnt vmcnt(18)
	v_mfma_f32_16x16x32_f16 v[70:73], v[154:157], v[134:137], v[70:73]
	s_waitcnt vmcnt(17)
	v_mfma_f32_16x16x32_f16 v[74:77], v[158:161], v[134:137], v[74:77]
	s_waitcnt vmcnt(16)
	v_mfma_f32_16x16x32_f16 v[78:81], v[162:165], v[134:137], v[78:81]
	s_waitcnt lgkmcnt(2)
	v_mfma_f32_16x16x32_f16 v[82:85], v[150:153], v[138:141], v[82:85]
	v_mfma_f32_16x16x32_f16 v[86:89], v[154:157], v[138:141], v[86:89]
	v_mfma_f32_16x16x32_f16 v[90:93], v[158:161], v[138:141], v[90:93]
	v_mfma_f32_16x16x32_f16 v[94:97], v[162:165], v[138:141], v[94:97]
	s_waitcnt lgkmcnt(1)
	v_mfma_f32_16x16x32_f16 v[98:101], v[150:153], v[142:145], v[98:101]
	v_mfma_f32_16x16x32_f16 v[102:105], v[154:157], v[142:145], v[102:105]
	v_mfma_f32_16x16x32_f16 v[106:109], v[158:161], v[142:145], v[106:109]
	v_mfma_f32_16x16x32_f16 v[110:113], v[162:165], v[142:145], v[110:113]
	s_waitcnt lgkmcnt(0)
	v_mfma_f32_16x16x32_f16 v[114:117], v[150:153], v[146:149], v[114:117]
	v_mfma_f32_16x16x32_f16 v[118:121], v[154:157], v[146:149], v[118:121]
	v_mfma_f32_16x16x32_f16 v[122:125], v[158:161], v[146:149], v[122:125]
	v_mfma_f32_16x16x32_f16 v[126:129], v[162:165], v[146:149], v[126:129]
	s_setprio 1
	s_add_i32 s5, s5, 6
	s_addk_i32 s4, 0x6000
	s_cmp_gt_u32 s5, 23
	s_cbranch_scc0 .LBB0_2
	v_lshrrev_b32_e32 v166, 2, v0
	v_and_b32_e32 v166, 12, v166
	v_and_b32_e32 v167, 0x1c0, v0
	v_or_b32_e32 v166, v167, v166
	v_lshlrev_b32_e32 v166, 2, v166
	global_load_dwordx4 v[150:153], v166, s[6:7]
	global_load_dwordx4 v[154:157], v166, s[6:7] offset:64
	global_load_dwordx4 v[158:161], v166, s[6:7] offset:128
	global_load_dwordx4 v[162:165], v166, s[6:7] offset:192
	s_waitcnt lgkmcnt(0)
	s_barrier
	ds_read_b128 v[134:137], v132
	ds_read_b128 v[138:141], v132 offset:2048
	ds_read_b128 v[142:145], v132 offset:4096
	ds_read_b128 v[146:149], v132 offset:6144
	s_setprio 2
	s_waitcnt vmcnt(19) lgkmcnt(3)
	v_mfma_f32_16x16x32_f16 v[50:53], v[54:57], v[134:137], v[50:53]
	s_waitcnt vmcnt(18)
	v_mfma_f32_16x16x32_f16 v[70:73], v[58:61], v[134:137], v[70:73]
	s_waitcnt vmcnt(17)
	v_mfma_f32_16x16x32_f16 v[74:77], v[62:65], v[134:137], v[74:77]
	s_waitcnt lgkmcnt(2)
	v_mfma_f32_16x16x32_f16 v[82:85], v[54:57], v[138:141], v[82:85]
	v_mfma_f32_16x16x32_f16 v[86:89], v[58:61], v[138:141], v[86:89]
	v_mfma_f32_16x16x32_f16 v[90:93], v[62:65], v[138:141], v[90:93]
	s_waitcnt lgkmcnt(1)
	v_mfma_f32_16x16x32_f16 v[98:101], v[54:57], v[142:145], v[98:101]
	v_mfma_f32_16x16x32_f16 v[102:105], v[58:61], v[142:145], v[102:105]
	v_mfma_f32_16x16x32_f16 v[106:109], v[62:65], v[142:145], v[106:109]
	s_waitcnt lgkmcnt(0)
	v_mfma_f32_16x16x32_f16 v[54:57], v[54:57], v[146:149], v[114:117]
	v_mfma_f32_16x16x32_f16 v[58:61], v[58:61], v[146:149], v[118:121]
	v_mfma_f32_16x16x32_f16 v[62:65], v[62:65], v[146:149], v[122:125]
	s_waitcnt vmcnt(16)
	v_mfma_f32_16x16x32_f16 v[78:81], v[66:69], v[134:137], v[78:81]
	v_mfma_f32_16x16x32_f16 v[94:97], v[66:69], v[138:141], v[94:97]
	v_mfma_f32_16x16x32_f16 v[110:113], v[66:69], v[142:145], v[110:113]
	v_mfma_f32_16x16x32_f16 v[66:69], v[66:69], v[146:149], v[126:129]
	s_setprio 1
	ds_read_b128 v[114:117], v132 offset:1024
	ds_read_b128 v[118:121], v132 offset:3072
	ds_read_b128 v[122:125], v132 offset:5120
	ds_read_b128 v[126:129], v132 offset:7168
	s_setprio 2
	s_waitcnt vmcnt(15) lgkmcnt(3)
	v_mfma_f32_16x16x32_f16 v[50:53], v[34:37], v[114:117], v[50:53]
	s_waitcnt vmcnt(14)
	v_mfma_f32_16x16x32_f16 v[70:73], v[38:41], v[114:117], v[70:73]
	s_waitcnt vmcnt(13)
	v_mfma_f32_16x16x32_f16 v[74:77], v[42:45], v[114:117], v[74:77]
	s_waitcnt vmcnt(12)
	v_mfma_f32_16x16x32_f16 v[78:81], v[46:49], v[114:117], v[78:81]
	s_waitcnt lgkmcnt(2)
	v_mfma_f32_16x16x32_f16 v[82:85], v[34:37], v[118:121], v[82:85]
	v_mfma_f32_16x16x32_f16 v[86:89], v[38:41], v[118:121], v[86:89]
	v_mfma_f32_16x16x32_f16 v[90:93], v[42:45], v[118:121], v[90:93]
	v_mfma_f32_16x16x32_f16 v[94:97], v[46:49], v[118:121], v[94:97]
	s_waitcnt lgkmcnt(1)
	v_mfma_f32_16x16x32_f16 v[98:101], v[34:37], v[122:125], v[98:101]
	v_mfma_f32_16x16x32_f16 v[102:105], v[38:41], v[122:125], v[102:105]
	v_mfma_f32_16x16x32_f16 v[106:109], v[42:45], v[122:125], v[106:109]
	v_mfma_f32_16x16x32_f16 v[110:113], v[46:49], v[122:125], v[110:113]
	s_waitcnt lgkmcnt(0)
	v_mfma_f32_16x16x32_f16 v[34:37], v[34:37], v[126:129], v[54:57]
	v_mfma_f32_16x16x32_f16 v[38:41], v[38:41], v[126:129], v[58:61]
	v_mfma_f32_16x16x32_f16 v[42:45], v[42:45], v[126:129], v[62:65]
	v_mfma_f32_16x16x32_f16 v[46:49], v[46:49], v[126:129], v[66:69]
	s_setprio 1
	s_waitcnt lgkmcnt(0)
	s_barrier
	ds_read_b128 v[54:57], v132 offset:8192
	ds_read_b128 v[58:61], v132 offset:10240
	ds_read_b128 v[62:65], v132 offset:12288
	ds_read_b128 v[66:69], v132 offset:14336
	s_setprio 2
	s_waitcnt vmcnt(11) lgkmcnt(3)
	v_mfma_f32_16x16x32_f16 v[50:53], v[30:33], v[54:57], v[50:53]
	s_waitcnt lgkmcnt(2)
	v_mfma_f32_16x16x32_f16 v[82:85], v[30:33], v[58:61], v[82:85]
	s_waitcnt vmcnt(10)
	v_mfma_f32_16x16x32_f16 v[86:89], v[18:21], v[58:61], v[86:89]
	s_waitcnt vmcnt(9)
	v_mfma_f32_16x16x32_f16 v[90:93], v[22:25], v[58:61], v[90:93]
	s_waitcnt vmcnt(8)
	v_mfma_f32_16x16x32_f16 v[58:61], v[26:29], v[58:61], v[94:97]
	s_waitcnt lgkmcnt(1)
	v_mfma_f32_16x16x32_f16 v[94:97], v[30:33], v[62:65], v[98:101]
	v_mfma_f32_16x16x32_f16 v[98:101], v[18:21], v[62:65], v[102:105]
	v_mfma_f32_16x16x32_f16 v[102:105], v[22:25], v[62:65], v[106:109]
	v_mfma_f32_16x16x32_f16 v[62:65], v[26:29], v[62:65], v[110:113]
	v_mfma_f32_16x16x32_f16 v[70:73], v[18:21], v[54:57], v[70:73]
	v_mfma_f32_16x16x32_f16 v[74:77], v[22:25], v[54:57], v[74:77]
	v_mfma_f32_16x16x32_f16 v[78:81], v[26:29], v[54:57], v[78:81]
	s_waitcnt lgkmcnt(0)
	v_mfma_f32_16x16x32_f16 v[106:109], v[30:33], v[66:69], v[34:37]
	v_mfma_f32_16x16x32_f16 v[110:113], v[18:21], v[66:69], v[38:41]
	v_mfma_f32_16x16x32_f16 v[114:117], v[22:25], v[66:69], v[42:45]
	v_mfma_f32_16x16x32_f16 v[66:69], v[26:29], v[66:69], v[46:49]
	s_setprio 1
	ds_read_b128 v[18:21], v132 offset:9216
	ds_read_b128 v[22:25], v132 offset:11264
	ds_read_b128 v[42:45], v132 offset:13312
	ds_read_b128 v[118:121], v132 offset:15360
	s_setprio 2
	s_waitcnt vmcnt(7) lgkmcnt(3)
	v_mfma_f32_16x16x32_f16 v[122:125], v[2:5], v[18:21], v[50:53]
	s_waitcnt vmcnt(6)
	v_mfma_f32_16x16x32_f16 v[54:57], v[6:9], v[18:21], v[70:73]
	s_waitcnt vmcnt(5)
	v_mfma_f32_16x16x32_f16 v[38:41], v[10:13], v[18:21], v[74:77]
	s_waitcnt vmcnt(4)
	v_mfma_f32_16x16x32_f16 v[26:29], v[14:17], v[18:21], v[78:81]
	s_waitcnt lgkmcnt(2)
	v_mfma_f32_16x16x32_f16 v[70:73], v[2:5], v[22:25], v[82:85]
	v_mfma_f32_16x16x32_f16 v[50:53], v[6:9], v[22:25], v[86:89]
	v_mfma_f32_16x16x32_f16 v[34:37], v[10:13], v[22:25], v[90:93]
	v_mfma_f32_16x16x32_f16 v[22:25], v[14:17], v[22:25], v[58:61]
	s_waitcnt lgkmcnt(1)
	v_mfma_f32_16x16x32_f16 v[74:77], v[2:5], v[42:45], v[94:97]
	v_mfma_f32_16x16x32_f16 v[46:49], v[6:9], v[42:45], v[98:101]
	v_mfma_f32_16x16x32_f16 v[30:33], v[10:13], v[42:45], v[102:105]
	v_mfma_f32_16x16x32_f16 v[18:21], v[14:17], v[42:45], v[62:65]
	s_waitcnt lgkmcnt(0)
	v_mfma_f32_16x16x32_f16 v[62:65], v[2:5], v[118:121], v[106:109]
	v_mfma_f32_16x16x32_f16 v[42:45], v[6:9], v[118:121], v[110:113]
	v_mfma_f32_16x16x32_f16 v[6:9], v[10:13], v[118:121], v[114:117]
	v_mfma_f32_16x16x32_f16 v[2:5], v[14:17], v[118:121], v[66:69]
	s_setprio 1
	s_ashr_i32 s3, s2, 31
	s_lshl_b64 s[12:13], s[2:3], 11
	s_add_u32 s4, s10, s12
	s_addc_u32 s5, s11, s13
	v_mov_b32_e32 v96, 0x3c800000
	v_mov_b32_e32 v97, 0x3c800000
	v_and_b32_e32 v1, 15, v0
	v_cmp_eq_u32_e32 vcc, 0, v1
	s_nop 7
	s_waitcnt vmcnt(0)
	v_pk_fma_f32 v[122:123], v[122:123], v[96:97], v[150:151]
	v_pk_fma_f32 v[124:125], v[124:125], v[96:97], v[152:153]
	v_max_f32_e32 v122, 0, v122
	v_max_f32_e32 v123, 0, v123
	v_max_f32_e32 v124, 0, v124
	v_max_f32_e32 v125, 0, v125
	v_pk_add_f32 v[80:81], v[122:123], 0 op_sel_hi:[1,0]
	v_pk_add_f32 v[82:83], v[124:125], 0 op_sel_hi:[1,0]
	v_pk_fma_f32 v[70:71], v[70:71], v[96:97], v[150:151]
	v_pk_fma_f32 v[72:73], v[72:73], v[96:97], v[152:153]
	v_max_f32_e32 v70, 0, v70
	v_max_f32_e32 v71, 0, v71
	v_max_f32_e32 v72, 0, v72
	v_max_f32_e32 v73, 0, v73
	v_pk_add_f32 v[80:81], v[80:81], v[70:71]
	v_pk_add_f32 v[82:83], v[82:83], v[72:73]
	v_pk_fma_f32 v[74:75], v[74:75], v[96:97], v[150:151]
	v_pk_fma_f32 v[76:77], v[76:77], v[96:97], v[152:153]
	v_max_f32_e32 v74, 0, v74
	v_max_f32_e32 v75, 0, v75
	v_max_f32_e32 v76, 0, v76
	v_max_f32_e32 v77, 0, v77
	v_pk_add_f32 v[80:81], v[80:81], v[74:75]
	v_pk_add_f32 v[82:83], v[82:83], v[76:77]
	v_pk_fma_f32 v[62:63], v[62:63], v[96:97], v[150:151]
	v_pk_fma_f32 v[64:65], v[64:65], v[96:97], v[152:153]
	v_max_f32_e32 v62, 0, v62
	v_max_f32_e32 v63, 0, v63
	v_max_f32_e32 v64, 0, v64
	v_max_f32_e32 v65, 0, v65
	v_pk_add_f32 v[80:81], v[80:81], v[62:63]
	v_pk_add_f32 v[82:83], v[82:83], v[64:65]
	v_pk_fma_f32 v[54:55], v[54:55], v[96:97], v[154:155]
	v_pk_fma_f32 v[56:57], v[56:57], v[96:97], v[156:157]
	v_max_f32_e32 v54, 0, v54
	v_max_f32_e32 v55, 0, v55
	v_max_f32_e32 v56, 0, v56
	v_max_f32_e32 v57, 0, v57
	v_pk_add_f32 v[84:85], v[54:55], 0 op_sel_hi:[1,0]
	v_pk_add_f32 v[86:87], v[56:57], 0 op_sel_hi:[1,0]
	v_pk_fma_f32 v[50:51], v[50:51], v[96:97], v[154:155]
	v_pk_fma_f32 v[52:53], v[52:53], v[96:97], v[156:157]
	v_max_f32_e32 v50, 0, v50
	v_max_f32_e32 v51, 0, v51
	v_max_f32_e32 v52, 0, v52
	v_max_f32_e32 v53, 0, v53
	v_pk_add_f32 v[84:85], v[84:85], v[50:51]
	v_pk_add_f32 v[86:87], v[86:87], v[52:53]
	v_pk_fma_f32 v[46:47], v[46:47], v[96:97], v[154:155]
	v_pk_fma_f32 v[48:49], v[48:49], v[96:97], v[156:157]
	v_max_f32_e32 v46, 0, v46
	v_max_f32_e32 v47, 0, v47
	v_max_f32_e32 v48, 0, v48
	v_max_f32_e32 v49, 0, v49
	v_pk_add_f32 v[84:85], v[84:85], v[46:47]
	v_pk_add_f32 v[86:87], v[86:87], v[48:49]
	v_pk_fma_f32 v[42:43], v[42:43], v[96:97], v[154:155]
	v_pk_fma_f32 v[44:45], v[44:45], v[96:97], v[156:157]
	v_max_f32_e32 v42, 0, v42
	v_max_f32_e32 v43, 0, v43
	v_max_f32_e32 v44, 0, v44
	v_max_f32_e32 v45, 0, v45
	v_pk_add_f32 v[84:85], v[84:85], v[42:43]
	v_pk_add_f32 v[86:87], v[86:87], v[44:45]
	v_pk_fma_f32 v[38:39], v[38:39], v[96:97], v[158:159]
	v_pk_fma_f32 v[40:41], v[40:41], v[96:97], v[160:161]
	v_max_f32_e32 v38, 0, v38
	v_max_f32_e32 v39, 0, v39
	v_max_f32_e32 v40, 0, v40
	v_max_f32_e32 v41, 0, v41
	v_pk_add_f32 v[88:89], v[38:39], 0 op_sel_hi:[1,0]
	v_pk_add_f32 v[90:91], v[40:41], 0 op_sel_hi:[1,0]
	v_pk_fma_f32 v[34:35], v[34:35], v[96:97], v[158:159]
	v_pk_fma_f32 v[36:37], v[36:37], v[96:97], v[160:161]
	v_max_f32_e32 v34, 0, v34
	v_max_f32_e32 v35, 0, v35
	v_max_f32_e32 v36, 0, v36
	v_max_f32_e32 v37, 0, v37
	v_pk_add_f32 v[88:89], v[88:89], v[34:35]
	v_pk_add_f32 v[90:91], v[90:91], v[36:37]
	v_pk_fma_f32 v[30:31], v[30:31], v[96:97], v[158:159]
	v_pk_fma_f32 v[32:33], v[32:33], v[96:97], v[160:161]
	v_max_f32_e32 v30, 0, v30
	v_max_f32_e32 v31, 0, v31
	v_max_f32_e32 v32, 0, v32
	v_max_f32_e32 v33, 0, v33
	v_pk_add_f32 v[88:89], v[88:89], v[30:31]
	v_pk_add_f32 v[90:91], v[90:91], v[32:33]
	v_pk_fma_f32 v[6:7], v[6:7], v[96:97], v[158:159]
	v_pk_fma_f32 v[8:9], v[8:9], v[96:97], v[160:161]
	v_max_f32_e32 v6, 0, v6
	v_max_f32_e32 v7, 0, v7
	v_max_f32_e32 v8, 0, v8
	v_max_f32_e32 v9, 0, v9
	v_pk_add_f32 v[88:89], v[88:89], v[6:7]
	v_pk_add_f32 v[90:91], v[90:91], v[8:9]
	v_pk_fma_f32 v[26:27], v[26:27], v[96:97], v[162:163]
	v_pk_fma_f32 v[28:29], v[28:29], v[96:97], v[164:165]
	v_max_f32_e32 v26, 0, v26
	v_max_f32_e32 v27, 0, v27
	v_max_f32_e32 v28, 0, v28
	v_max_f32_e32 v29, 0, v29
	v_pk_add_f32 v[92:93], v[26:27], 0 op_sel_hi:[1,0]
	v_pk_add_f32 v[94:95], v[28:29], 0 op_sel_hi:[1,0]
	v_pk_fma_f32 v[22:23], v[22:23], v[96:97], v[162:163]
	v_pk_fma_f32 v[24:25], v[24:25], v[96:97], v[164:165]
	v_max_f32_e32 v22, 0, v22
	v_max_f32_e32 v23, 0, v23
	v_max_f32_e32 v24, 0, v24
	v_max_f32_e32 v25, 0, v25
	v_pk_add_f32 v[92:93], v[92:93], v[22:23]
	v_pk_add_f32 v[94:95], v[94:95], v[24:25]
	v_pk_fma_f32 v[18:19], v[18:19], v[96:97], v[162:163]
	v_pk_fma_f32 v[20:21], v[20:21], v[96:97], v[164:165]
	v_max_f32_e32 v18, 0, v18
	v_max_f32_e32 v19, 0, v19
	v_max_f32_e32 v20, 0, v20
	v_max_f32_e32 v21, 0, v21
	v_pk_add_f32 v[92:93], v[92:93], v[18:19]
	v_pk_add_f32 v[94:95], v[94:95], v[20:21]
	v_pk_fma_f32 v[2:3], v[2:3], v[96:97], v[162:163]
	v_pk_fma_f32 v[4:5], v[4:5], v[96:97], v[164:165]
	v_max_f32_e32 v2, 0, v2
	v_max_f32_e32 v3, 0, v3
	v_max_f32_e32 v4, 0, v4
	v_max_f32_e32 v5, 0, v5
	v_pk_add_f32 v[92:93], v[92:93], v[2:3]
	v_pk_add_f32 v[94:95], v[94:95], v[4:5]
	v_add_f32_dpp v80, v80, v80 quad_perm:[1,0,3,2] row_mask:0xf bank_mask:0xf
	v_add_f32_dpp v81, v81, v81 quad_perm:[1,0,3,2] row_mask:0xf bank_mask:0xf
	v_add_f32_dpp v82, v82, v82 quad_perm:[1,0,3,2] row_mask:0xf bank_mask:0xf
	v_add_f32_dpp v83, v83, v83 quad_perm:[1,0,3,2] row_mask:0xf bank_mask:0xf
	v_add_f32_dpp v84, v84, v84 quad_perm:[1,0,3,2] row_mask:0xf bank_mask:0xf
	v_add_f32_dpp v85, v85, v85 quad_perm:[1,0,3,2] row_mask:0xf bank_mask:0xf
	v_add_f32_dpp v86, v86, v86 quad_perm:[1,0,3,2] row_mask:0xf bank_mask:0xf
	v_add_f32_dpp v87, v87, v87 quad_perm:[1,0,3,2] row_mask:0xf bank_mask:0xf
	v_add_f32_dpp v88, v88, v88 quad_perm:[1,0,3,2] row_mask:0xf bank_mask:0xf
	v_add_f32_dpp v89, v89, v89 quad_perm:[1,0,3,2] row_mask:0xf bank_mask:0xf
	v_add_f32_dpp v90, v90, v90 quad_perm:[1,0,3,2] row_mask:0xf bank_mask:0xf
	v_add_f32_dpp v91, v91, v91 quad_perm:[1,0,3,2] row_mask:0xf bank_mask:0xf
	v_add_f32_dpp v92, v92, v92 quad_perm:[1,0,3,2] row_mask:0xf bank_mask:0xf
	v_add_f32_dpp v93, v93, v93 quad_perm:[1,0,3,2] row_mask:0xf bank_mask:0xf
	v_add_f32_dpp v94, v94, v94 quad_perm:[1,0,3,2] row_mask:0xf bank_mask:0xf
	v_add_f32_dpp v95, v95, v95 quad_perm:[1,0,3,2] row_mask:0xf bank_mask:0xf
	v_add_f32_dpp v80, v80, v80 quad_perm:[2,3,0,1] row_mask:0xf bank_mask:0xf
	v_add_f32_dpp v81, v81, v81 quad_perm:[2,3,0,1] row_mask:0xf bank_mask:0xf
	v_add_f32_dpp v82, v82, v82 quad_perm:[2,3,0,1] row_mask:0xf bank_mask:0xf
	v_add_f32_dpp v83, v83, v83 quad_perm:[2,3,0,1] row_mask:0xf bank_mask:0xf
	v_add_f32_dpp v84, v84, v84 quad_perm:[2,3,0,1] row_mask:0xf bank_mask:0xf
	v_add_f32_dpp v85, v85, v85 quad_perm:[2,3,0,1] row_mask:0xf bank_mask:0xf
	v_add_f32_dpp v86, v86, v86 quad_perm:[2,3,0,1] row_mask:0xf bank_mask:0xf
	v_add_f32_dpp v87, v87, v87 quad_perm:[2,3,0,1] row_mask:0xf bank_mask:0xf
	v_add_f32_dpp v88, v88, v88 quad_perm:[2,3,0,1] row_mask:0xf bank_mask:0xf
	v_add_f32_dpp v89, v89, v89 quad_perm:[2,3,0,1] row_mask:0xf bank_mask:0xf
	v_add_f32_dpp v90, v90, v90 quad_perm:[2,3,0,1] row_mask:0xf bank_mask:0xf
	v_add_f32_dpp v91, v91, v91 quad_perm:[2,3,0,1] row_mask:0xf bank_mask:0xf
	v_add_f32_dpp v92, v92, v92 quad_perm:[2,3,0,1] row_mask:0xf bank_mask:0xf
	v_add_f32_dpp v93, v93, v93 quad_perm:[2,3,0,1] row_mask:0xf bank_mask:0xf
	v_add_f32_dpp v94, v94, v94 quad_perm:[2,3,0,1] row_mask:0xf bank_mask:0xf
	v_add_f32_dpp v95, v95, v95 quad_perm:[2,3,0,1] row_mask:0xf bank_mask:0xf
	v_add_f32_dpp v80, v80, v80 row_half_mirror row_mask:0xf bank_mask:0xf
	v_add_f32_dpp v81, v81, v81 row_half_mirror row_mask:0xf bank_mask:0xf
	v_add_f32_dpp v82, v82, v82 row_half_mirror row_mask:0xf bank_mask:0xf
	v_add_f32_dpp v83, v83, v83 row_half_mirror row_mask:0xf bank_mask:0xf
	v_add_f32_dpp v84, v84, v84 row_half_mirror row_mask:0xf bank_mask:0xf
	v_add_f32_dpp v85, v85, v85 row_half_mirror row_mask:0xf bank_mask:0xf
	v_add_f32_dpp v86, v86, v86 row_half_mirror row_mask:0xf bank_mask:0xf
	v_add_f32_dpp v87, v87, v87 row_half_mirror row_mask:0xf bank_mask:0xf
	v_add_f32_dpp v88, v88, v88 row_half_mirror row_mask:0xf bank_mask:0xf
	v_add_f32_dpp v89, v89, v89 row_half_mirror row_mask:0xf bank_mask:0xf
	v_add_f32_dpp v90, v90, v90 row_half_mirror row_mask:0xf bank_mask:0xf
	v_add_f32_dpp v91, v91, v91 row_half_mirror row_mask:0xf bank_mask:0xf
	v_add_f32_dpp v92, v92, v92 row_half_mirror row_mask:0xf bank_mask:0xf
	v_add_f32_dpp v93, v93, v93 row_half_mirror row_mask:0xf bank_mask:0xf
	v_add_f32_dpp v94, v94, v94 row_half_mirror row_mask:0xf bank_mask:0xf
	v_add_f32_dpp v95, v95, v95 row_half_mirror row_mask:0xf bank_mask:0xf
	v_add_f32_dpp v80, v80, v80 row_mirror row_mask:0xf bank_mask:0xf
	v_add_f32_dpp v81, v81, v81 row_mirror row_mask:0xf bank_mask:0xf
	v_add_f32_dpp v82, v82, v82 row_mirror row_mask:0xf bank_mask:0xf
	v_add_f32_dpp v83, v83, v83 row_mirror row_mask:0xf bank_mask:0xf
	v_add_f32_dpp v84, v84, v84 row_mirror row_mask:0xf bank_mask:0xf
	v_add_f32_dpp v85, v85, v85 row_mirror row_mask:0xf bank_mask:0xf
	v_add_f32_dpp v86, v86, v86 row_mirror row_mask:0xf bank_mask:0xf
	v_add_f32_dpp v87, v87, v87 row_mirror row_mask:0xf bank_mask:0xf
	v_add_f32_dpp v88, v88, v88 row_mirror row_mask:0xf bank_mask:0xf
	v_add_f32_dpp v89, v89, v89 row_mirror row_mask:0xf bank_mask:0xf
	v_add_f32_dpp v90, v90, v90 row_mirror row_mask:0xf bank_mask:0xf
	v_add_f32_dpp v91, v91, v91 row_mirror row_mask:0xf bank_mask:0xf
	v_add_f32_dpp v92, v92, v92 row_mirror row_mask:0xf bank_mask:0xf
	v_add_f32_dpp v93, v93, v93 row_mirror row_mask:0xf bank_mask:0xf
	v_add_f32_dpp v94, v94, v94 row_mirror row_mask:0xf bank_mask:0xf
	v_add_f32_dpp v95, v95, v95 row_mirror row_mask:0xf bank_mask:0xf
	s_and_saveexec_b64 s[6:7], vcc
	global_store_dwordx4 v166, v[80:83], s[4:5]
	global_store_dwordx4 v166, v[84:87], s[4:5] offset:64
	global_store_dwordx4 v166, v[88:91], s[4:5] offset:128
	global_store_dwordx4 v166, v[92:95], s[4:5] offset:192
